# nca kernels: v_rcp_f32 instead of IEEE div sequences in merge/sigmoid/softmax3; wave max via permlane16/32 swap instead of 2 ds_bpermute round trips
# speedup vs baseline: 1.0163x; 1.0163x over previous
.LBB1_16:
	s_or_b64 exec, exec, s[2:3]
	s_movk_i32 s2, 0x168
	s_waitcnt vmcnt(4)
	v_and_b32_e32 v39, 63, v0
	v_and_b32_e32 v40, 15, v0
	v_lshlrev_b32_e32 v26, 3, v50
	v_cmp_gt_u32_e32 vcc, s2, v0
	s_and_saveexec_b64 s[2:3], vcc
	s_movk_i32 s4, 0xa0
	v_mad_u32_u24 v27, v0, s4, 0
	v_mov_b32_e32 v28, 0x3c00
	ds_write_b16 v27, v28 offset:144
	s_or_b64 exec, exec, s[2:3]
	v_lshlrev_b32_e32 v38, 2, v50
	v_or_b32_e32 v28, s21, v63
	v_add_u32_e32 v29, v28, v38
	v_sub_u32_e32 v30, v38, v61
	s_movk_i32 s7, 0x80
	v_cmp_gt_u32_e64 s[2:3], 11, v30
	v_cmp_gt_u32_e64 s[4:5], s7, v29
	v_or_b32_e32 v29, 1, v38
	s_and_b64 s[2:3], s[2:3], s[4:5]
	v_mov_b32_e32 v111, 0xff800000
	v_add_u32_e32 v30, v28, v29
	v_sub_u32_e32 v29, v29, v61
	v_cndmask_b32_e64 v112, v111, 0, s[2:3]
	v_cmp_gt_u32_e64 s[2:3], 11, v29
	v_cmp_gt_u32_e64 s[4:5], s7, v30
	v_or_b32_e32 v29, 2, v38
	v_lshrrev_b32_e32 v110, 8, v0
	s_and_b64 s[2:3], s[2:3], s[4:5]
	v_add_u32_e32 v30, v28, v29
	v_sub_u32_e32 v29, v29, v61
	v_cndmask_b32_e64 v113, v111, 0, s[2:3]
	v_cmp_gt_u32_e64 s[2:3], 11, v29
	v_or_b32_e32 v29, 3, v38
	v_mad_u32_u24 v41, v110, 7, v62
	v_cmp_gt_u32_e64 s[4:5], s7, v30
	v_add_u32_e32 v28, v28, v29
	v_mad_u32_u24 v98, v41, 20, v63
	s_and_b64 s[2:3], s[2:3], s[4:5]
	v_cmp_gt_u32_e64 s[4:5], s7, v28
	v_add_u32_e32 v28, v98, v40
	s_movk_i32 s6, 0xa0
	v_mul_lo_u32 v28, v28, s6
	v_add_u32_e32 v99, 0, v28
	v_mul_u32_u24_e32 v27, 7, v110
	v_sub_u32_e32 v29, v29, v61
	v_lshl_add_u32 v94, v26, 1, v99
	s_waitcnt lgkmcnt(0)
	s_barrier
	v_cndmask_b32_e64 v114, v111, 0, s[2:3]
	v_cmp_gt_u32_e64 s[2:3], 11, v29
	v_sub_u32_e32 v31, v27, v1
	ds_read_b128 v[26:29], v94
	v_or_b32_e32 v116, s20, v62
	s_and_b64 s[2:3], s[2:3], s[4:5]
	v_mad_u32_u24 v30, v110, 7, v116
	ds_read_b128 v[34:37], v94 offset:64
	v_cndmask_b32_e64 v115, v111, 0, s[2:3]
	v_cmp_gt_u32_e64 s[2:3], 11, v31
	v_cmp_gt_u32_e64 s[4:5], s7, v30
	s_and_b64 s[2:3], s[2:3], s[4:5]
	v_cndmask_b32_e64 v30, v111, v112, s[2:3]
	v_cndmask_b32_e64 v33, v111, v115, s[2:3]
	v_cndmask_b32_e64 v32, v111, v114, s[2:3]
	v_cndmask_b32_e64 v31, v111, v113, s[2:3]
	v_cmp_gt_u32_e32 vcc, 16, v39
	v_add_u32_e32 v98, v98, v38
	s_waitcnt lgkmcnt(1)
	v_mfma_f32_16x16x32_f16 v[30:33], v[26:29], v[10:13], v[30:33]
	ds_read_b128 v[42:45], v99 offset:128
	ds_read_b128 v[46:49], v94 offset:3200
	v_cndmask_b32_e32 v29, 0, v25, vcc
	s_waitcnt lgkmcnt(2)
	v_mfma_f32_16x16x32_f16 v[30:33], v[34:37], v[2:5], v[30:33]
	v_cndmask_b32_e32 v28, 0, v24, vcc
	v_cndmask_b32_e32 v27, 0, v23, vcc
	v_cndmask_b32_e32 v26, 0, v22, vcc
	ds_read_b128 v[34:37], v94 offset:3264
	ds_read_b128 v[50:53], v99 offset:3328
	s_waitcnt lgkmcnt(3)
	v_mfma_f32_16x16x32_f16 v[22:25], v[42:45], v[26:29], v[30:33]
	ds_read_b128 v[42:45], v94 offset:6400
	ds_read_b128 v[62:65], v94 offset:6464
	v_or_b32_e32 v98, v98, v1
	v_mad_u32_u24 v30, v110, 7, 1
	v_add_u32_e32 v31, v116, v30
	v_sub_u32_e32 v30, v30, v1
	v_cmp_gt_u32_e32 vcc, 11, v30
	v_cmp_gt_u32_e64 s[2:3], s7, v31
	s_and_b64 vcc, vcc, s[2:3]
	v_cndmask_b32_e32 v30, v111, v112, vcc
	v_cndmask_b32_e32 v33, v111, v115, vcc
	v_cndmask_b32_e32 v32, v111, v114, vcc
	v_cndmask_b32_e32 v31, v111, v113, vcc
	v_mul_lo_u32 v98, v98, s6
	v_lshlrev_b32_e32 v61, 3, v61
	s_waitcnt lgkmcnt(4)
	v_mfma_f32_16x16x32_f16 v[30:33], v[46:49], v[10:13], v[30:33]
	ds_read_b128 v[46:49], v99 offset:6528
	ds_read_b128 v[66:69], v94 offset:9600
	v_add3_u32 v61, 0, v98, v61
	s_waitcnt lgkmcnt(5)
	v_mfma_f32_16x16x32_f16 v[30:33], v[34:37], v[2:5], v[30:33]
	v_mad_u32_u24 v34, v110, 7, 2
	v_add_u32_e32 v35, v116, v34
	v_sub_u32_e32 v34, v34, v1
	v_cmp_gt_u32_e32 vcc, 11, v34
	v_cmp_gt_u32_e64 s[2:3], s7, v35
	s_and_b64 vcc, vcc, s[2:3]
	v_cndmask_b32_e32 v34, v111, v112, vcc
	v_cndmask_b32_e32 v37, v111, v115, vcc
	v_cndmask_b32_e32 v36, v111, v114, vcc
	v_cndmask_b32_e32 v35, v111, v113, vcc
	ds_read_b128 v[70:73], v94 offset:9664
	ds_read_b128 v[74:77], v99 offset:9728
	s_waitcnt lgkmcnt(6)
	v_mfma_f32_16x16x32_f16 v[30:33], v[50:53], v[26:29], v[30:33]
	ds_read_b128 v[50:53], v94 offset:12800
	ds_read_b128 v[78:81], v94 offset:12864
	s_waitcnt vmcnt(3)
	v_cvt_pk_f16_f32 v21, v20, v21
	s_waitcnt lgkmcnt(7)
	v_mfma_f32_16x16x32_f16 v[34:37], v[42:45], v[10:13], v[34:37]
	ds_read_b128 v[42:45], v99 offset:12928
	ds_read_b128 v[82:85], v94 offset:16000
	v_cvt_pk_f16_f32 v20, v18, v19
	s_waitcnt lgkmcnt(8)
	v_mfma_f32_16x16x32_f16 v[34:37], v[62:65], v[2:5], v[34:37]
	ds_read_b128 v[62:65], v94 offset:16064
	ds_read_b128 v[86:89], v99 offset:16128
	v_mul_u32_u24_e32 v18, 0xa0, v60
	s_waitcnt lgkmcnt(9)
	v_mfma_f32_16x16x32_f16 v[34:37], v[46:49], v[26:29], v[34:37]
	v_mad_u32_u24 v46, v110, 7, 3
	v_add_u32_e32 v47, v116, v46
	v_sub_u32_e32 v46, v46, v1
	v_cmp_gt_u32_e32 vcc, 11, v46
	v_cmp_gt_u32_e64 s[2:3], s7, v47
	s_and_b64 vcc, vcc, s[2:3]
	v_cndmask_b32_e32 v46, v111, v112, vcc
	v_cndmask_b32_e32 v49, v111, v115, vcc
	v_cndmask_b32_e32 v48, v111, v114, vcc
	v_cndmask_b32_e32 v47, v111, v113, vcc
	ds_read_b128 v[90:93], v94 offset:19200
	ds_read_b128 v[94:97], v94 offset:19264
	s_waitcnt lgkmcnt(10)
	v_mfma_f32_16x16x32_f16 v[46:49], v[66:69], v[10:13], v[46:49]
	ds_read_b128 v[66:69], v99 offset:19328
	ds_read_b64_tr_b16 v[100:101], v61 offset:3200
	v_lshlrev_b32_e32 v19, 1, v56
	s_waitcnt lgkmcnt(11)
	v_mfma_f32_16x16x32_f16 v[46:49], v[70:73], v[2:5], v[46:49]
	v_mad_u32_u24 v72, v110, 7, 4
	v_add_u32_e32 v73, v116, v72
	v_sub_u32_e32 v72, v72, v1
	v_cmp_gt_u32_e32 vcc, 11, v72
	v_cmp_gt_u32_e64 s[2:3], s7, v73
	s_and_b64 vcc, vcc, s[2:3]
	ds_read_b64_tr_b16 v[98:99], v61
	ds_read_b64_tr_b16 v[70:71], v61 offset:32
	s_waitcnt lgkmcnt(12)
	v_mfma_f32_16x16x32_f16 v[46:49], v[74:77], v[26:29], v[46:49]
	v_cndmask_b32_e32 v74, v111, v112, vcc
	v_cndmask_b32_e32 v77, v111, v115, vcc
	v_cndmask_b32_e32 v76, v111, v114, vcc
	v_cndmask_b32_e32 v75, v111, v113, vcc
	ds_read_b64_tr_b16 v[72:73], v61 offset:3232
	ds_read_b64_tr_b16 v[102:103], v61 offset:64
	s_waitcnt lgkmcnt(13)
	v_mfma_f32_16x16x32_f16 v[50:53], v[50:53], v[10:13], v[74:77]
	ds_read_b64_tr_b16 v[104:105], v61 offset:3264
	v_add3_u32 v18, 0, v18, v19
	s_movk_i32 s4, 0xe39
	ds_read_b64_tr_b16 v[74:75], v61 offset:96
	s_waitcnt lgkmcnt(14)
	v_mfma_f32_16x16x32_f16 v[50:53], v[78:81], v[2:5], v[50:53]
	ds_read_b64_tr_b16 v[76:77], v61 offset:3296
	ds_read_b64_tr_b16 v[78:79], v61 offset:128
	s_movk_i32 s5, 0xffee
	s_waitcnt lgkmcnt(14)
	v_mfma_f32_16x16x32_f16 v[42:45], v[42:45], v[26:29], v[50:53]
	ds_read_b64_tr_b16 v[80:81], v61 offset:3328
	ds_read_b64_tr_b16 v[106:107], v61 offset:6400
	s_waitcnt vmcnt(2)
	v_cvt_pk_f16_f32 v17, v16, v17
	v_mad_u32_u24 v50, v110, 7, 5
	v_add_u32_e32 v51, v116, v50
	v_sub_u32_e32 v50, v50, v1
	v_cmp_gt_u32_e32 vcc, 11, v50
	v_cmp_gt_u32_e64 s[2:3], s7, v51
	s_and_b64 vcc, vcc, s[2:3]
	v_cndmask_b32_e32 v50, v111, v112, vcc
	v_cndmask_b32_e32 v53, v111, v115, vcc
	v_cndmask_b32_e32 v52, v111, v114, vcc
	v_cndmask_b32_e32 v51, v111, v113, vcc
	v_cvt_pk_f16_f32 v16, v14, v15
	s_nop 0
	v_mfma_f32_16x16x32_f16 v[50:53], v[82:85], v[10:13], v[50:53]
	ds_read_b64_tr_b16 v[108:109], v61 offset:9600
	ds_read_b64_tr_b16 v[82:83], v61 offset:6432
	s_waitcnt lgkmcnt(14)
	v_mfma_f32_16x16x32_f16 v[50:53], v[62:65], v[2:5], v[50:53]
	v_mad_u32_u24 v64, v110, 7, 6
	v_add_u32_e32 v65, v116, v64
	v_sub_u32_e32 v64, v64, v1
	v_cmp_gt_u32_e32 vcc, 11, v64
	v_cmp_gt_u32_e64 s[2:3], s7, v65
	s_and_b64 vcc, vcc, s[2:3]
	ds_read_b64_tr_b16 v[84:85], v61 offset:9632
	ds_read_b64_tr_b16 v[62:63], v61 offset:6464
	v_mfma_f32_16x16x32_f16 v[50:53], v[86:89], v[26:29], v[50:53]
	v_cndmask_b32_e32 v86, v111, v112, vcc
	v_cndmask_b32_e32 v89, v111, v115, vcc
	v_cndmask_b32_e32 v88, v111, v114, vcc
	v_cndmask_b32_e32 v87, v111, v113, vcc
	ds_read_b64_tr_b16 v[64:65], v61 offset:9664
	ds_read_b64_tr_b16 v[110:111], v61 offset:6496
	v_mfma_f32_16x16x32_f16 v[10:13], v[90:93], v[10:13], v[86:89]
	s_mov_b32 s2, 0xff800000
	ds_read_b64_tr_b16 v[112:113], v61 offset:9696
	s_nop 0
	ds_read_b64_tr_b16 v[86:87], v61 offset:6528
	v_mfma_f32_16x16x32_f16 v[2:5], v[94:97], v[2:5], v[10:13]
	ds_read_b64_tr_b16 v[88:89], v61 offset:9728
	s_nop 1
	v_max3_f32 v12, v22, s2, v23
	v_max3_f32 v12, v12, v24, v25
	v_max3_f32 v12, v12, v30, v31
	v_max3_f32 v12, v12, v32, v33
	v_max3_f32 v12, v12, v34, v35
	v_max3_f32 v12, v12, v36, v37
	v_max3_f32 v12, v12, v46, v47
	v_max3_f32 v12, v12, v48, v49
	v_mbcnt_lo_u32_b32 v13, -1, 0
	ds_read_b64_tr_b16 v[10:11], v61 offset:12800
	s_waitcnt lgkmcnt(14)
	v_mfma_f32_16x16x32_f16 v[2:5], v[66:69], v[26:29], v[2:5]
	v_max3_f32 v12, v12, v42, v43
	v_mbcnt_hi_u32_b32 v13, -1, v13
	v_max3_f32 v12, v12, v44, v45
	v_and_b32_e32 v27, 64, v13
	v_max3_f32 v12, v12, v50, v51
	v_xor_b32_e32 v26, 16, v13
	v_add_u32_e32 v27, 64, v27
	v_max3_f32 v12, v12, v52, v53
	v_cmp_lt_i32_e32 vcc, v26, v27
	v_max3_f32 v12, v12, v2, v3
	v_max3_f32 v12, v12, v4, v5
	v_mov_b32_e32 v26, v12
	s_load_dwordx2 s[2:3], s[0:1], 0x20
	s_movk_i32 s0, 0x510
	v_permlane16_swap_b32_e32 v12, v26
	v_cmp_gt_u32_e32 vcc, 11, v41
	v_mov_b32_e32 v41, 0xc80
	v_max_f32_e32 v12, v12, v26
	v_mov_b32_e32 v13, v12
	s_nop 1
	v_permlane32_swap_b32_e32 v12, v13
	s_waitcnt lgkmcnt(0)
	s_nop 0
	v_max_f32_e32 v26, v12, v13
	v_sub_f32_e32 v29, v34, v26
	v_exp_f32_e32 v92, v29
	v_sub_f32_e32 v29, v35, v26
	v_exp_f32_e32 v93, v29
	v_sub_f32_e32 v29, v36, v26
	v_exp_f32_e32 v36, v29
	v_sub_f32_e32 v29, v37, v26
	v_exp_f32_e32 v37, v29
	v_sub_f32_e32 v29, v46, v26
	v_exp_f32_e32 v94, v29
	v_sub_f32_e32 v29, v47, v26
	v_exp_f32_e32 v95, v29
	v_sub_f32_e32 v29, v48, v26
	v_sub_f32_e32 v13, v23, v26
	v_sub_f32_e32 v23, v25, v26
	v_sub_f32_e32 v25, v31, v26
	v_exp_f32_e32 v96, v29
	v_sub_f32_e32 v29, v49, v26
	v_sub_f32_e32 v12, v22, v26
	v_sub_f32_e32 v22, v24, v26
	v_sub_f32_e32 v24, v30, v26
	v_exp_f32_e32 v27, v25
	v_sub_f32_e32 v25, v32, v26
	v_sub_f32_e32 v28, v33, v26
	v_exp_f32_e32 v97, v29
	v_sub_f32_e32 v29, v42, v26
	v_exp_f32_e32 v12, v12
	v_exp_f32_e32 v13, v13
	v_exp_f32_e32 v22, v22
	v_exp_f32_e32 v23, v23
	v_exp_f32_e32 v24, v24
	v_exp_f32_e32 v25, v25
	v_exp_f32_e32 v28, v28
	v_exp_f32_e32 v114, v29
	v_sub_f32_e32 v29, v43, v26
	v_exp_f32_e32 v115, v29
	v_sub_f32_e32 v29, v44, v26
	v_exp_f32_e32 v116, v29
	v_sub_f32_e32 v29, v45, v26
	v_exp_f32_e32 v117, v29
	v_sub_f32_e32 v29, v50, v26
	v_exp_f32_e32 v118, v29
	v_sub_f32_e32 v29, v51, v26
	v_cvt_pk_f16_f32 v25, v25, v28
	v_cvt_pk_f16_f32 v24, v24, v27
	v_cvt_pk_f16_f32 v23, v22, v23
	v_cvt_pk_f16_f32 v22, v12, v13
	v_exp_f32_e32 v119, v29
	v_cndmask_b32_e32 v41, 0, v41, vcc
	v_mfma_f32_16x16x32_f16 v[28:31], v[98:101], v[22:25], 0
	ds_read_b64_tr_b16 v[12:13], v61 offset:16000
	ds_read_b64_tr_b16 v[32:33], v61 offset:12832
	v_sub_f32_e32 v27, v52, v26
	v_mfma_f32_16x16x32_f16 v[42:45], v[70:73], v[22:25], 0
	ds_read_b64_tr_b16 v[34:35], v61 offset:16032
	ds_read_b64_tr_b16 v[46:47], v61 offset:12864
	v_exp_f32_e32 v27, v27
	v_mfma_f32_16x16x32_f16 v[66:69], v[102:105], v[22:25], 0
	ds_read_b64_tr_b16 v[48:49], v61 offset:16064
	ds_read_b64_tr_b16 v[70:71], v61 offset:12896
	v_sub_f32_e32 v2, v2, v26
	v_mfma_f32_16x16x32_f16 v[74:77], v[74:77], v[22:25], 0
	ds_read_b64_tr_b16 v[72:73], v61 offset:16096
	ds_read_b64_tr_b16 v[90:91], v61 offset:12928
	v_cmp_gt_u32_e32 vcc, s0, v58
	v_mfma_f32_16x16x32_f16 v[22:25], v[78:81], v[22:25], 0
	v_cvt_pk_f16_f32 v78, v92, v93
	ds_read_b64_tr_b16 v[92:93], v61 offset:16128
	v_cvt_pk_f16_f32 v81, v96, v97
	v_cvt_pk_f16_f32 v80, v94, v95
	v_cvt_pk_f16_f32 v79, v36, v37
	v_add_u32_e32 v36, v61, v41
	v_sub_f32_e32 v37, v53, v26
	ds_read_b64_tr_b16 v[94:95], v61 offset:19200
	v_mfma_f32_16x16x32_f16 v[28:31], v[106:109], v[78:81], v[28:31]
	ds_read_b64_tr_b16 v[96:97], v36 offset:19200
	ds_read_b64_tr_b16 v[100:101], v36 offset:19232
	v_exp_f32_e32 v37, v37
	v_mfma_f32_16x16x32_f16 v[42:45], v[82:85], v[78:81], v[42:45]
	ds_read_b64_tr_b16 v[98:99], v61 offset:19232
	ds_read_b64_tr_b16 v[50:51], v61 offset:19264
	v_mfma_f32_16x16x32_f16 v[62:65], v[62:65], v[78:81], v[66:69]
	ds_read_b64_tr_b16 v[52:53], v36 offset:19264
	s_nop 1
	ds_read_b64_tr_b16 v[66:67], v61 offset:19296
	v_mfma_f32_16x16x32_f16 v[74:77], v[110:113], v[78:81], v[74:77]
	ds_read_b64_tr_b16 v[68:69], v36 offset:19296
	ds_read_b64_tr_b16 v[82:83], v61 offset:19328
	v_mfma_f32_16x16x32_f16 v[22:25], v[86:89], v[78:81], v[22:25]
	ds_read_b64_tr_b16 v[84:85], v36 offset:19328
	ds_write_b64 v18, v[20:21] offset:57600
	v_mul_u32_u24_sdwa v18, v59, s4 dst_sel:DWORD dst_unused:UNUSED_PAD src0_sel:WORD_0 src1_sel:DWORD
	v_mul_i32_i24_sdwa v19, v18, s5 dst_sel:DWORD dst_unused:UNUSED_PAD src0_sel:WORD_1 src1_sel:DWORD
	v_mul_u32_u24_sdwa v14, v18, s6 dst_sel:DWORD dst_unused:UNUSED_PAD src0_sel:WORD_1 src1_sel:DWORD
	v_add_lshl_u32 v15, v19, v59, 3
	v_exp_f32_e32 v18, v2
	v_sub_f32_e32 v19, v3, v26
	v_sub_f32_e32 v2, v4, v26
	v_sub_f32_e32 v21, v5, v26
	v_cvt_pk_f16_f32 v81, v27, v37
	v_cvt_pk_f16_f32 v80, v118, v119
	v_cvt_pk_f16_f32 v79, v116, v117
	v_cvt_pk_f16_f32 v78, v114, v115
	v_add3_u32 v14, 0, v14, v15
	v_exp_f32_e32 v20, v2
	v_exp_f32_e32 v21, v21
	v_exp_f32_e32 v19, v19
	s_waitcnt lgkmcnt(14)
	v_mfma_f32_16x16x32_f16 v[10:13], v[10:13], v[78:81], v[28:31]
	ds_write_b64 v14, v[16:17] offset:57600
	v_mfma_f32_16x16x32_f16 v[14:17], v[32:35], v[78:81], v[42:45]
	v_mfma_f32_16x16x32_f16 v[28:31], v[46:49], v[78:81], v[62:65]
	s_nop 1
	v_mov_b32_e32 v44, 0
	v_cvt_pk_f16_f32 v43, v20, v21
	v_cvt_pk_f16_f32 v42, v18, v19
	s_waitcnt lgkmcnt(14)
	v_mfma_f32_16x16x32_f16 v[2:5], v[70:73], v[78:81], v[74:77]
	v_mov_b32_e32 v45, v44
	s_waitcnt lgkmcnt(12)
	v_mfma_f32_16x16x32_f16 v[32:35], v[90:93], v[78:81], v[22:25]
	s_waitcnt lgkmcnt(10)
	v_mfma_f32_16x16x32_f16 v[22:25], v[94:97], v[42:45], v[10:13]
	s_waitcnt lgkmcnt(8)
	v_mfma_f32_16x16x32_f16 v[18:21], v[98:101], v[42:45], v[14:17]
	s_waitcnt lgkmcnt(6)
	v_mfma_f32_16x16x32_f16 v[14:17], v[50:53], v[42:45], v[28:31]
	s_waitcnt lgkmcnt(4)
	v_mfma_f32_16x16x32_f16 v[10:13], v[66:69], v[42:45], v[2:5]
	s_waitcnt lgkmcnt(2)
	v_mfma_f32_16x16x32_f16 v[2:5], v[82:85], v[42:45], v[32:35]
	s_and_saveexec_b64 s[0:1], vcc
	s_cbranch_execz .LBB1_20
	v_mul_u32_u24_sdwa v27, v58, s4 dst_sel:DWORD dst_unused:UNUSED_PAD src0_sel:WORD_0 src1_sel:DWORD
	v_mul_i32_i24_sdwa v28, v27, s5 dst_sel:DWORD dst_unused:UNUSED_PAD src0_sel:WORD_1 src1_sel:DWORD
	s_waitcnt vmcnt(1)
	v_cvt_pk_f16_f32 v9, v8, v9
	v_cvt_pk_f16_f32 v8, v6, v7
	v_mul_u32_u24_sdwa v6, v27, s6 dst_sel:DWORD dst_unused:UNUSED_PAD src0_sel:WORD_1 src1_sel:DWORD
	v_add_lshl_u32 v7, v28, v58, 3
	v_add3_u32 v6, 0, v6, v7
	ds_write_b64 v6, v[8:9] offset:57600

.LBB1_22:
	s_or_b64 exec, exec, s[0:1]
	s_add_i32 s0, 0, 0x11880
	s_movk_i32 s1, 0x1600
	v_mov_b32_e32 v7, s0
	v_mad_u32_u24 v8, v6, s1, v7
	v_lshlrev_b32_e32 v9, 2, v39
	v_xor_b32_e32 v6, 4, v6
	v_add_u32_e32 v27, v8, v9
	v_mad_u32_u24 v6, v6, s1, v7
	ds_write2st64_b32 v27, v22, v23 offset1:1
	ds_write2st64_b32 v27, v24, v25 offset0:2 offset1:3
	ds_write2st64_b32 v27, v18, v19 offset0:4 offset1:5
	ds_write2st64_b32 v27, v20, v21 offset0:6 offset1:7
	ds_write2st64_b32 v27, v14, v15 offset0:8 offset1:9
	ds_write2st64_b32 v27, v16, v17 offset0:10 offset1:11
	ds_write2st64_b32 v27, v10, v11 offset0:12 offset1:13
	ds_write2st64_b32 v27, v12, v13 offset0:14 offset1:15
	ds_write2st64_b32 v27, v2, v3 offset0:16 offset1:17
	ds_write2st64_b32 v27, v4, v5 offset0:18 offset1:19
	ds_write_b32 v27, v26 offset:5120
	v_add_u32_e32 v27, v6, v9
	s_waitcnt lgkmcnt(0)
	s_barrier
	ds_read_b32 v9, v27 offset:5120
	v_lshlrev_b32_e32 v7, 2, v40
	v_add_u32_e32 v8, v8, v7
	v_add_u32_e32 v6, v6, v7
	ds_read_b32 v7, v6 offset:4224
	ds_read_b32 v6, v8 offset:4224
	ds_read2st64_b32 v[32:33], v27 offset0:18 offset1:19
	s_waitcnt lgkmcnt(3)
	v_max_f32_e32 v8, v9, v9
	v_max_f32_e32 v28, v26, v26
	v_max_f32_e32 v28, v28, v8
	v_sub_f32_e32 v8, v26, v28
	v_sub_f32_e32 v9, v9, v28
	v_exp_f32_e32 v8, v8
	v_exp_f32_e32 v9, v9
	s_movk_i32 s0, 0x100
	s_add_i32 s1, 0, 0x10e00
	v_lshl_add_u32 v26, v38, 2, s1
	s_waitcnt lgkmcnt(1)
	v_pk_mul_f32 v[6:7], v[6:7], v[8:9]
	v_cmp_gt_u32_e64 s[0:1], s0, v0
	v_add_f32_e32 v6, v6, v7
	v_rcp_f32_e32 v6, v6
	v_cndmask_b32_e64 v56, 48, 0, s[0:1]
	v_lshl_add_u32 v41, v56, 2, v26
	ds_read_b128 v[28:31], v41
	ds_read2st64_b32 v[34:35], v27 offset0:16 offset1:17
	v_mul_f32_e32 v36, v8, v6
	v_mul_f32_e32 v40, v9, v6
	ds_read2st64_b32 v[6:7], v27 offset1:1
	ds_read2st64_b32 v[8:9], v27 offset0:2 offset1:3
	ds_read2st64_b32 v[42:43], v27 offset0:4 offset1:5
	ds_read2st64_b32 v[44:45], v27 offset0:6 offset1:7
	ds_read2st64_b32 v[46:47], v27 offset0:8 offset1:9
	ds_read2st64_b32 v[48:49], v27 offset0:10 offset1:11
	ds_read2st64_b32 v[50:51], v27 offset0:12 offset1:13
	ds_read2st64_b32 v[52:53], v27 offset0:14 offset1:15
	s_waitcnt lgkmcnt(7)
	v_pk_mul_f32 v[6:7], v[40:41], v[6:7] op_sel_hi:[0,1]
	s_waitcnt lgkmcnt(6)
	v_pk_mul_f32 v[8:9], v[40:41], v[8:9] op_sel_hi:[0,1]
	v_pk_fma_f32 v[6:7], v[36:37], v[22:23], v[6:7] op_sel_hi:[0,1,1]
	v_pk_fma_f32 v[8:9], v[36:37], v[24:25], v[8:9] op_sel_hi:[0,1,1]
	v_cvt_pk_f16_f32 v6, v6, v7
	v_cvt_pk_f16_f32 v7, v8, v9
	s_waitcnt lgkmcnt(5)
	v_pk_mul_f32 v[8:9], v[40:41], v[42:43] op_sel_hi:[0,1]
	v_pk_fma_f32 v[8:9], v[36:37], v[18:19], v[8:9] op_sel_hi:[0,1,1]
	s_waitcnt lgkmcnt(4)
	v_pk_mul_f32 v[18:19], v[40:41], v[44:45] op_sel_hi:[0,1]
	v_pk_fma_f32 v[18:19], v[36:37], v[20:21], v[18:19] op_sel_hi:[0,1,1]
	v_cvt_pk_f16_f32 v8, v8, v9
	v_cvt_pk_f16_f32 v9, v18, v19
	s_waitcnt lgkmcnt(3)
	v_pk_mul_f32 v[18:19], v[40:41], v[46:47] op_sel_hi:[0,1]
	v_pk_fma_f32 v[14:15], v[36:37], v[14:15], v[18:19] op_sel_hi:[0,1,1]
	s_waitcnt lgkmcnt(2)
	v_pk_mul_f32 v[18:19], v[40:41], v[48:49] op_sel_hi:[0,1]
	v_pk_fma_f32 v[16:17], v[36:37], v[16:17], v[18:19] op_sel_hi:[0,1,1]
	v_cvt_pk_f16_f32 v14, v14, v15
	v_cvt_pk_f16_f32 v15, v16, v17
	s_waitcnt lgkmcnt(1)
	v_pk_mul_f32 v[16:17], v[40:41], v[50:51] op_sel_hi:[0,1]
	v_pk_fma_f32 v[10:11], v[36:37], v[10:11], v[16:17] op_sel_hi:[0,1,1]
	v_cvt_pk_f16_f32 v16, v10, v11
	s_waitcnt lgkmcnt(0)
	v_pk_mul_f32 v[10:11], v[40:41], v[52:53] op_sel_hi:[0,1]
	v_lshlrev_b32_e32 v0, 2, v0
	v_pk_fma_f32 v[10:11], v[36:37], v[12:13], v[10:11] op_sel_hi:[0,1,1]
	v_and_b32_e32 v20, 12, v0
	v_cvt_pk_f16_f32 v17, v10, v11
	v_pk_mul_f32 v[10:11], v[40:41], v[34:35] op_sel_hi:[0,1]
	v_or_b32_e32 v0, v56, v20
	v_pk_fma_f32 v[2:3], v[36:37], v[2:3], v[10:11] op_sel_hi:[0,1,1]
	v_lshlrev_b32_e32 v27, 1, v0
	v_or_b32_e32 v0, v1, v38
	v_cvt_pk_f16_f32 v10, v2, v3
	v_pk_mul_f32 v[2:3], v[40:41], v[32:33] op_sel_hi:[0,1]
	v_mul_u32_u24_e32 v0, 0x50, v0
	v_pk_fma_f32 v[2:3], v[36:37], v[4:5], v[2:3] op_sel_hi:[0,1,1]
	v_lshlrev_b32_e32 v21, 1, v0
	v_cvt_pk_f16_f32 v2, v2, v3
	v_cmp_gt_u32_e32 vcc, 32, v39
	v_add3_u32 v42, 0, v27, v21
	v_add_u32_e32 v22, 0, v21
	v_cndmask_b32_e32 v25, 0, v2, vcc
	v_add_u32_e32 v43, v22, v27
	ds_read_b64_tr_b16 v[2:3], v42 offset:57600
	ds_read_b64_tr_b16 v[4:5], v43 offset:60160
	v_and_or_b32 v0, v38, 4, v1
	s_movk_i32 s4, 0xa0
	v_mad_u32_u24 v0, v0, s4, 0
	v_add_u32_e32 v23, 0xe100, v0
	v_lshl_add_u64 v[18:19], v[54:55], 1, s[2:3]
	v_lshlrev_b32_e32 v32, 1, v38
	v_mov_b32_e32 v33, 0
	s_waitcnt lgkmcnt(0)
	v_mfma_f32_16x16x32_f16 v[0:3], v[2:5], v[6:9], v[28:31]
	v_lshl_add_u64 v[4:5], v[18:19], 0, v[32:33]
	v_add_u32_e32 v18, v23, v27
	v_cndmask_b32_e32 v24, 0, v10, vcc
	ds_read_b64_tr_b16 v[12:13], v43 offset:65280
	ds_read_b64_tr_b16 v[10:11], v42 offset:62720
	ds_read_b64_tr_b16 v[30:31], v18 offset:10240
	v_mov_b32_e32 v32, v33
	ds_read_b64_tr_b16 v[34:35], v42 offset:57632
	ds_read_b64_tr_b16 v[36:37], v43 offset:60192
	ds_read_b128 v[38:41], v41 offset:64
	s_waitcnt lgkmcnt(4)
	v_mfma_f32_16x16x32_f16 v[10:13], v[10:13], v[14:17], v[0:3]
	s_mov_b32 s2, 0xffff
	s_or_b64 s[4:5], s[0:1], vcc
	s_nop 0
	v_bfi_b32 v0, s2, v24, v24
	v_bfi_b32 v1, s2, v25, v25
	v_mov_b32_e32 v2, v33
	v_mov_b32_e32 v3, v33
	s_waitcnt lgkmcnt(0)
	v_mfma_f32_16x16x32_f16 v[34:37], v[34:37], v[6:9], v[38:41]
	v_mfma_f32_16x16x32_f16 v[10:13], v[30:33], v[0:3], v[10:13]
	ds_read_b64_tr_b16 v[44:45], v43 offset:65312
	ds_read_b64_tr_b16 v[42:43], v42 offset:62752
	ds_read_b64_tr_b16 v[30:31], v18 offset:10272
	v_lshlrev_b32_e32 v32, 1, v56
	v_lshl_add_u64 v[18:19], v[4:5], 0, v[32:33]
	v_mov_b32_e32 v32, v33
	s_waitcnt lgkmcnt(1)
	v_mfma_f32_16x16x32_f16 v[34:37], v[42:45], v[14:17], v[34:37]
	v_cvt_pk_f16_f32 v13, v12, v13
	v_cvt_pk_f16_f32 v12, v10, v11
	global_store_dwordx2 v[18:19], v[12:13], off
	s_waitcnt lgkmcnt(0)
	v_mfma_f32_16x16x32_f16 v[10:13], v[30:33], v[0:3], v[34:37]
	s_and_saveexec_b64 s[2:3], s[4:5]
	s_cbranch_execnz .LBB1_25
	s_or_b64 exec, exec, s[2:3]
	s_and_saveexec_b64 s[2:3], s[0:1]
	s_cbranch_execnz .LBB1_26

.LBB2_16:
	s_or_b64 exec, exec, s[2:3]
	s_movk_i32 s2, 0x168
	s_waitcnt vmcnt(12)
	v_and_b32_e32 v38, 63, v0
	v_lshlrev_b32_e32 v26, 3, v50
	v_cmp_gt_u32_e32 vcc, s2, v0
	s_and_saveexec_b64 s[2:3], vcc
	s_movk_i32 s4, 0xa0
	v_mad_u32_u24 v27, v0, s4, 0
	v_mov_b32_e32 v28, 0x3c00
	ds_write_b16 v27, v28 offset:144
	s_or_b64 exec, exec, s[2:3]
	v_lshlrev_b32_e32 v39, 2, v50
	v_or_b32_e32 v28, s30, v57
	v_add_u32_e32 v29, v28, v39
	v_sub_u32_e32 v30, v39, v1
	s_movk_i32 s7, 0x80
	v_cmp_gt_u32_e64 s[2:3], 11, v30
	v_cmp_gt_u32_e64 s[4:5], s7, v29
	v_or_b32_e32 v29, 1, v39
	s_and_b64 s[2:3], s[2:3], s[4:5]
	v_mov_b32_e32 v51, 0xff800000
	v_add_u32_e32 v30, v28, v29
	v_sub_u32_e32 v29, v29, v1
	v_cndmask_b32_e64 v52, v51, 0, s[2:3]
	v_cmp_gt_u32_e64 s[2:3], 11, v29
	v_cmp_gt_u32_e64 s[4:5], s7, v30
	v_or_b32_e32 v29, 2, v39
	v_lshrrev_b32_e32 v41, 8, v0
	s_and_b64 s[2:3], s[2:3], s[4:5]
	v_add_u32_e32 v30, v28, v29
	v_sub_u32_e32 v29, v29, v1
	v_cndmask_b32_e64 v53, v51, 0, s[2:3]
	v_cmp_gt_u32_e64 s[2:3], 11, v29
	v_or_b32_e32 v29, 3, v39
	v_mad_u32_u24 v40, v41, 7, v76
	v_cmp_gt_u32_e64 s[4:5], s7, v30
	v_add_u32_e32 v28, v28, v29
	v_mad_u32_u24 v116, v40, 20, v57
	s_and_b64 s[2:3], s[2:3], s[4:5]
	v_cmp_gt_u32_e64 s[4:5], s7, v28
	v_add_u32_e32 v28, v116, v59
	s_movk_i32 s6, 0xa0
	v_mul_lo_u32 v28, v28, s6
	v_add_u32_e32 v117, 0, v28
	v_mul_u32_u24_e32 v27, 7, v41
	v_sub_u32_e32 v29, v29, v1
	v_lshl_add_u32 v112, v26, 1, v117
	s_waitcnt lgkmcnt(0)
	s_barrier
	v_cndmask_b32_e64 v128, v51, 0, s[2:3]
	v_cmp_gt_u32_e64 s[2:3], 11, v29
	v_sub_u32_e32 v31, v27, v60
	ds_read_b128 v[26:29], v112
	v_or_b32_e32 v130, s29, v76
	s_and_b64 s[2:3], s[2:3], s[4:5]
	v_mad_u32_u24 v30, v41, 7, v130
	ds_read_b128 v[34:37], v112 offset:64
	v_cndmask_b32_e64 v129, v51, 0, s[2:3]
	v_cmp_gt_u32_e64 s[2:3], 11, v31
	v_cmp_gt_u32_e64 s[4:5], s7, v30
	s_and_b64 s[2:3], s[2:3], s[4:5]
	v_cndmask_b32_e64 v30, v51, v52, s[2:3]
	v_cndmask_b32_e64 v33, v51, v129, s[2:3]
	v_cndmask_b32_e64 v32, v51, v128, s[2:3]
	v_cndmask_b32_e64 v31, v51, v53, s[2:3]
	v_cmp_gt_u32_e32 vcc, 16, v38
	v_add_u32_e32 v116, v116, v39
	s_waitcnt lgkmcnt(1)
	v_mfma_f32_16x16x32_f16 v[30:33], v[26:29], v[10:13], v[30:33]
	ds_read_b128 v[42:45], v117 offset:128
	ds_read_b128 v[46:49], v112 offset:3200
	v_cndmask_b32_e32 v29, 0, v25, vcc
	s_waitcnt lgkmcnt(2)
	v_mfma_f32_16x16x32_f16 v[30:33], v[34:37], v[2:5], v[30:33]
	v_cndmask_b32_e32 v28, 0, v24, vcc
	v_cndmask_b32_e32 v27, 0, v23, vcc
	v_cndmask_b32_e32 v26, 0, v22, vcc
	ds_read_b128 v[34:37], v112 offset:3264
	ds_read_b128 v[76:79], v117 offset:3328
	s_waitcnt lgkmcnt(3)
	v_mfma_f32_16x16x32_f16 v[22:25], v[42:45], v[26:29], v[30:33]
	ds_read_b128 v[42:45], v112 offset:6400
	ds_read_b128 v[80:83], v112 offset:6464
	v_or_b32_e32 v116, v116, v60
	v_mad_u32_u24 v30, v41, 7, 1
	v_add_u32_e32 v31, v130, v30
	v_sub_u32_e32 v30, v30, v60
	v_cmp_gt_u32_e32 vcc, 11, v30
	v_cmp_gt_u32_e64 s[2:3], s7, v31
	s_and_b64 vcc, vcc, s[2:3]
	v_cndmask_b32_e32 v30, v51, v52, vcc
	v_cndmask_b32_e32 v33, v51, v129, vcc
	v_cndmask_b32_e32 v32, v51, v128, vcc
	v_cndmask_b32_e32 v31, v51, v53, vcc
	v_mul_lo_u32 v116, v116, s6
	s_waitcnt vmcnt(11)
	v_cvt_pk_f16_f32 v21, v20, v21
	s_waitcnt lgkmcnt(4)
	v_mfma_f32_16x16x32_f16 v[30:33], v[46:49], v[10:13], v[30:33]
	ds_read_b128 v[46:49], v117 offset:6528
	ds_read_b128 v[84:87], v112 offset:9600
	v_cvt_pk_f16_f32 v20, v18, v19
	s_waitcnt lgkmcnt(5)
	v_mfma_f32_16x16x32_f16 v[30:33], v[34:37], v[2:5], v[30:33]
	v_mad_u32_u24 v34, v41, 7, 2
	v_add_u32_e32 v35, v130, v34
	v_sub_u32_e32 v34, v34, v60
	v_cmp_gt_u32_e32 vcc, 11, v34
	v_cmp_gt_u32_e64 s[2:3], s7, v35
	s_and_b64 vcc, vcc, s[2:3]
	v_cndmask_b32_e32 v34, v51, v52, vcc
	v_cndmask_b32_e32 v37, v51, v129, vcc
	v_cndmask_b32_e32 v36, v51, v128, vcc
	v_cndmask_b32_e32 v35, v51, v53, vcc
	ds_read_b128 v[88:91], v112 offset:9664
	ds_read_b128 v[92:95], v117 offset:9728
	s_waitcnt lgkmcnt(6)
	v_mfma_f32_16x16x32_f16 v[30:33], v[76:79], v[26:29], v[30:33]
	ds_read_b128 v[76:79], v112 offset:12800
	ds_read_b128 v[96:99], v112 offset:12864
	v_mul_u32_u24_e32 v18, 0xa0, v75
	s_waitcnt lgkmcnt(7)
	v_mfma_f32_16x16x32_f16 v[34:37], v[42:45], v[10:13], v[34:37]
	ds_read_b128 v[42:45], v117 offset:12928
	ds_read_b128 v[100:103], v112 offset:16000
	v_lshlrev_b32_e32 v19, 1, v54
	s_waitcnt lgkmcnt(8)
	v_mfma_f32_16x16x32_f16 v[34:37], v[80:83], v[2:5], v[34:37]
	ds_read_b128 v[80:83], v112 offset:16064
	ds_read_b128 v[104:107], v117 offset:16128
	v_add3_u32 v18, 0, v18, v19
	s_waitcnt lgkmcnt(9)
	v_mfma_f32_16x16x32_f16 v[34:37], v[46:49], v[26:29], v[34:37]
	v_mad_u32_u24 v46, v41, 7, 3
	v_add_u32_e32 v47, v130, v46
	v_sub_u32_e32 v46, v46, v60
	v_cmp_gt_u32_e32 vcc, 11, v46
	v_cmp_gt_u32_e64 s[2:3], s7, v47
	s_and_b64 vcc, vcc, s[2:3]
	v_cndmask_b32_e32 v46, v51, v52, vcc
	v_cndmask_b32_e32 v49, v51, v129, vcc
	v_cndmask_b32_e32 v48, v51, v128, vcc
	v_cndmask_b32_e32 v47, v51, v53, vcc
	ds_read_b128 v[108:111], v112 offset:19200
	ds_read_b128 v[112:115], v112 offset:19264
	s_waitcnt lgkmcnt(10)
	v_mfma_f32_16x16x32_f16 v[46:49], v[84:87], v[10:13], v[46:49]
	ds_read_b128 v[84:87], v117 offset:19328
	v_lshlrev_b32_e32 v117, 3, v1
	v_add3_u32 v132, 0, v116, v117
	ds_read_b64_tr_b16 v[118:119], v132 offset:3200
	s_waitcnt lgkmcnt(11)
	v_mfma_f32_16x16x32_f16 v[46:49], v[88:91], v[2:5], v[46:49]
	v_mad_u32_u24 v90, v41, 7, 4
	v_add_u32_e32 v91, v130, v90
	v_sub_u32_e32 v90, v90, v60
	v_cmp_gt_u32_e32 vcc, 11, v90
	v_cmp_gt_u32_e64 s[2:3], s7, v91
	s_and_b64 vcc, vcc, s[2:3]
	ds_read_b64_tr_b16 v[116:117], v132
	ds_read_b64_tr_b16 v[88:89], v132 offset:32
	s_waitcnt lgkmcnt(12)
	v_mfma_f32_16x16x32_f16 v[46:49], v[92:95], v[26:29], v[46:49]
	v_cndmask_b32_e32 v92, v51, v52, vcc
	v_cndmask_b32_e32 v95, v51, v129, vcc
	v_cndmask_b32_e32 v94, v51, v128, vcc
	v_cndmask_b32_e32 v93, v51, v53, vcc
	ds_read_b64_tr_b16 v[90:91], v132 offset:3232
	ds_read_b64_tr_b16 v[120:121], v132 offset:64
	s_waitcnt lgkmcnt(13)
	v_mfma_f32_16x16x32_f16 v[76:79], v[76:79], v[10:13], v[92:95]
	ds_read_b64_tr_b16 v[122:123], v132 offset:3264
	s_movk_i32 s8, 0xffee
	s_waitcnt vmcnt(10)
	v_cvt_pk_f16_f32 v17, v16, v17
	ds_read_b64_tr_b16 v[92:93], v132 offset:96
	s_waitcnt lgkmcnt(14)
	v_mfma_f32_16x16x32_f16 v[76:79], v[96:99], v[2:5], v[76:79]
	ds_read_b64_tr_b16 v[94:95], v132 offset:3296
	ds_read_b64_tr_b16 v[96:97], v132 offset:128
	v_cvt_pk_f16_f32 v16, v14, v15
	s_waitcnt lgkmcnt(14)
	v_mfma_f32_16x16x32_f16 v[42:45], v[42:45], v[26:29], v[76:79]
	ds_read_b64_tr_b16 v[98:99], v132 offset:3328
	ds_read_b64_tr_b16 v[124:125], v132 offset:6400
	s_movk_i32 s4, 0x510
	v_mad_u32_u24 v76, v41, 7, 5
	v_add_u32_e32 v77, v130, v76
	v_sub_u32_e32 v76, v76, v60
	v_cmp_gt_u32_e32 vcc, 11, v76
	v_cmp_gt_u32_e64 s[2:3], s7, v77
	s_and_b64 vcc, vcc, s[2:3]
	v_cndmask_b32_e32 v76, v51, v52, vcc
	v_cndmask_b32_e32 v79, v51, v129, vcc
	v_cndmask_b32_e32 v78, v51, v128, vcc
	v_cndmask_b32_e32 v77, v51, v53, vcc
	v_mad_u32_u24 v41, v41, 7, 6
	s_nop 0
	v_mfma_f32_16x16x32_f16 v[76:79], v[100:103], v[10:13], v[76:79]
	ds_read_b64_tr_b16 v[126:127], v132 offset:9600
	ds_read_b64_tr_b16 v[100:101], v132 offset:6432
	s_waitcnt lgkmcnt(14)
	v_mfma_f32_16x16x32_f16 v[76:79], v[80:83], v[2:5], v[76:79]
	v_add_u32_e32 v82, v130, v41
	v_sub_u32_e32 v41, v41, v60
	v_cmp_gt_u32_e32 vcc, 11, v41
	v_cmp_gt_u32_e64 s[2:3], s7, v82
	s_and_b64 vcc, vcc, s[2:3]
	ds_read_b64_tr_b16 v[102:103], v132 offset:9632
	ds_read_b64_tr_b16 v[80:81], v132 offset:6464
	v_mfma_f32_16x16x32_f16 v[76:79], v[104:107], v[26:29], v[76:79]
	v_cndmask_b32_e32 v104, v51, v52, vcc
	v_cndmask_b32_e32 v107, v51, v129, vcc
	v_cndmask_b32_e32 v106, v51, v128, vcc
	v_cndmask_b32_e32 v105, v51, v53, vcc
	ds_read_b64_tr_b16 v[82:83], v132 offset:9664
	ds_read_b64_tr_b16 v[128:129], v132 offset:6496
	v_mfma_f32_16x16x32_f16 v[10:13], v[108:111], v[10:13], v[104:107]
	s_mov_b32 s2, 0xff800000
	ds_read_b64_tr_b16 v[130:131], v132 offset:9696
	s_movk_i32 s7, 0xe39
	ds_read_b64_tr_b16 v[104:105], v132 offset:6528
	v_mfma_f32_16x16x32_f16 v[2:5], v[112:115], v[2:5], v[10:13]
	ds_read_b64_tr_b16 v[106:107], v132 offset:9728
	s_nop 1
	v_max3_f32 v12, v22, s2, v23
	v_max3_f32 v12, v12, v24, v25
	v_max3_f32 v12, v12, v30, v31
	v_max3_f32 v12, v12, v32, v33
	v_max3_f32 v12, v12, v34, v35
	v_max3_f32 v12, v12, v36, v37
	v_max3_f32 v12, v12, v46, v47
	v_max3_f32 v12, v12, v48, v49
	v_mbcnt_lo_u32_b32 v13, -1, 0
	ds_read_b64_tr_b16 v[10:11], v132 offset:12800
	s_waitcnt lgkmcnt(14)
	v_mfma_f32_16x16x32_f16 v[2:5], v[84:87], v[26:29], v[2:5]
	v_max3_f32 v12, v12, v42, v43
	v_mbcnt_hi_u32_b32 v13, -1, v13
	v_max3_f32 v12, v12, v44, v45
	v_and_b32_e32 v27, 64, v13
	v_max3_f32 v12, v12, v76, v77
	v_xor_b32_e32 v26, 16, v13
	v_add_u32_e32 v27, 64, v27
	v_max3_f32 v12, v12, v78, v79
	v_cmp_lt_i32_e32 vcc, v26, v27
	v_max3_f32 v12, v12, v2, v3
	v_max3_f32 v12, v12, v4, v5
	v_mov_b32_e32 v26, v12
	v_cmp_lt_u32_e64 s[2:3], 15, v38
	s_nop 0
	v_permlane16_swap_b32_e32 v12, v26
	v_cmp_gt_u32_e32 vcc, 11, v40
	s_nop 0
	v_max_f32_e32 v12, v12, v26
	v_mov_b32_e32 v13, v12
	s_nop 1
	v_permlane32_swap_b32_e32 v12, v13
	s_waitcnt lgkmcnt(0)
	s_nop 0
	v_max_f32_e32 v28, v12, v13
	v_sub_f32_e32 v12, v22, v28
	v_sub_f32_e32 v22, v24, v28
	v_sub_f32_e32 v24, v30, v28
	v_sub_f32_e32 v30, v35, v28
	v_exp_f32_e32 v41, v30
	v_sub_f32_e32 v30, v36, v28
	v_exp_f32_e32 v51, v30
	v_sub_f32_e32 v30, v37, v28
	v_exp_f32_e32 v52, v30
	v_sub_f32_e32 v30, v46, v28
	v_exp_f32_e32 v53, v30
	v_sub_f32_e32 v30, v47, v28
	v_exp_f32_e32 v110, v30
	v_sub_f32_e32 v30, v48, v28
	v_sub_f32_e32 v13, v23, v28
	v_sub_f32_e32 v23, v25, v28
	v_sub_f32_e32 v25, v31, v28
	v_exp_f32_e32 v111, v30
	v_sub_f32_e32 v30, v49, v28
	v_exp_f32_e32 v26, v25
	v_sub_f32_e32 v25, v32, v28
	v_sub_f32_e32 v27, v33, v28
	v_exp_f32_e32 v112, v30
	v_sub_f32_e32 v30, v42, v28
	v_exp_f32_e32 v12, v12
	v_exp_f32_e32 v13, v13
	v_exp_f32_e32 v22, v22
	v_exp_f32_e32 v23, v23
	v_exp_f32_e32 v24, v24
	v_exp_f32_e32 v25, v25
	v_exp_f32_e32 v27, v27
	v_exp_f32_e32 v133, v30
	v_sub_f32_e32 v30, v43, v28
	v_exp_f32_e32 v134, v30
	v_sub_f32_e32 v30, v44, v28
	v_exp_f32_e32 v135, v30
	v_sub_f32_e32 v30, v45, v28
	v_sub_f32_e32 v29, v34, v28
	v_exp_f32_e32 v136, v30
	v_sub_f32_e32 v30, v76, v28
	v_exp_f32_e32 v29, v29
	v_exp_f32_e32 v137, v30
	v_sub_f32_e32 v30, v77, v28
	v_cvt_pk_f16_f32 v25, v25, v27
	v_cvt_pk_f16_f32 v24, v24, v26
	v_cvt_pk_f16_f32 v23, v22, v23
	v_cvt_pk_f16_f32 v22, v12, v13
	v_exp_f32_e32 v138, v30
	v_mov_b32_e32 v27, 0xc80
	v_mfma_f32_16x16x32_f16 v[30:33], v[116:119], v[22:25], 0
	ds_read_b64_tr_b16 v[12:13], v132 offset:16000
	ds_read_b64_tr_b16 v[34:35], v132 offset:12832
	v_cndmask_b32_e32 v27, 0, v27, vcc
	v_mfma_f32_16x16x32_f16 v[42:45], v[88:91], v[22:25], 0
	ds_read_b64_tr_b16 v[36:37], v132 offset:16032
	ds_read_b64_tr_b16 v[46:47], v132 offset:12864
	v_sub_f32_e32 v26, v78, v28
	v_mfma_f32_16x16x32_f16 v[84:87], v[120:123], v[22:25], 0
	ds_read_b64_tr_b16 v[48:49], v132 offset:16064
	ds_read_b64_tr_b16 v[88:89], v132 offset:12896
	v_add_u32_e32 v27, v132, v27
	v_mfma_f32_16x16x32_f16 v[92:95], v[92:95], v[22:25], 0
	ds_read_b64_tr_b16 v[90:91], v132 offset:16096
	ds_read_b64_tr_b16 v[108:109], v132 offset:12928
	v_exp_f32_e32 v26, v26
	v_mfma_f32_16x16x32_f16 v[22:25], v[96:99], v[22:25], 0
	v_cvt_pk_f16_f32 v99, v111, v112
	v_cvt_pk_f16_f32 v98, v53, v110
	ds_read_b64_tr_b16 v[110:111], v132 offset:16128
	v_cvt_pk_f16_f32 v97, v51, v52
	v_cvt_pk_f16_f32 v96, v29, v41
	v_sub_f32_e32 v29, v79, v28
	ds_read_b64_tr_b16 v[112:113], v132 offset:19200
	v_mfma_f32_16x16x32_f16 v[30:33], v[124:127], v[96:99], v[30:33]
	ds_read_b64_tr_b16 v[114:115], v27 offset:19200
	ds_read_b64_tr_b16 v[118:119], v27 offset:19232
	v_exp_f32_e32 v29, v29
	v_mfma_f32_16x16x32_f16 v[40:43], v[100:103], v[96:99], v[42:45]
	ds_read_b64_tr_b16 v[116:117], v132 offset:19232
	ds_read_b64_tr_b16 v[76:77], v132 offset:19264
	v_sub_f32_e32 v2, v2, v28
	v_mfma_f32_16x16x32_f16 v[80:83], v[80:83], v[96:99], v[84:87]
	ds_read_b64_tr_b16 v[78:79], v27 offset:19264
	v_cmp_gt_u32_e32 vcc, s4, v61
	s_nop 0
	ds_read_b64_tr_b16 v[84:85], v132 offset:19296
	v_mfma_f32_16x16x32_f16 v[92:95], v[128:131], v[96:99], v[92:95]
	ds_read_b64_tr_b16 v[86:87], v27 offset:19296
	ds_read_b64_tr_b16 v[100:101], v132 offset:19328
	v_mfma_f32_16x16x32_f16 v[22:25], v[104:107], v[96:99], v[22:25]
	ds_read_b64_tr_b16 v[102:103], v27 offset:19328
	ds_write_b64 v18, v[20:21] offset:57600
	v_mul_u32_u24_sdwa v18, v62, s7 dst_sel:DWORD dst_unused:UNUSED_PAD src0_sel:WORD_0 src1_sel:DWORD
	v_mul_i32_i24_sdwa v19, v18, s8 dst_sel:DWORD dst_unused:UNUSED_PAD src0_sel:WORD_1 src1_sel:DWORD
	v_mul_u32_u24_sdwa v14, v18, s6 dst_sel:DWORD dst_unused:UNUSED_PAD src0_sel:WORD_1 src1_sel:DWORD
	v_add_lshl_u32 v15, v19, v62, 3
	v_exp_f32_e32 v18, v2
	v_sub_f32_e32 v19, v3, v28
	v_sub_f32_e32 v2, v4, v28
	v_sub_f32_e32 v21, v5, v28
	v_cvt_pk_f16_f32 v99, v26, v29
	v_cvt_pk_f16_f32 v98, v137, v138
	v_cvt_pk_f16_f32 v97, v135, v136
	v_cvt_pk_f16_f32 v96, v133, v134
	v_add3_u32 v14, 0, v14, v15
	v_exp_f32_e32 v20, v2
	v_exp_f32_e32 v21, v21
	v_exp_f32_e32 v19, v19
	s_waitcnt lgkmcnt(14)
	v_mfma_f32_16x16x32_f16 v[10:13], v[10:13], v[96:99], v[30:33]
	ds_write_b64 v14, v[16:17] offset:57600
	v_mfma_f32_16x16x32_f16 v[14:17], v[34:37], v[96:99], v[40:43]
	v_mfma_f32_16x16x32_f16 v[30:33], v[46:49], v[96:99], v[80:83]
	s_nop 1
	v_mov_b32_e32 v42, 0
	v_cvt_pk_f16_f32 v41, v20, v21
	v_cvt_pk_f16_f32 v40, v18, v19
	s_waitcnt lgkmcnt(14)
	v_mfma_f32_16x16x32_f16 v[2:5], v[88:91], v[96:99], v[92:95]
	v_mov_b32_e32 v43, v42
	s_waitcnt lgkmcnt(12)
	v_mfma_f32_16x16x32_f16 v[34:37], v[108:111], v[96:99], v[22:25]
	s_waitcnt lgkmcnt(10)
	v_mfma_f32_16x16x32_f16 v[22:25], v[112:115], v[40:43], v[10:13]
	s_waitcnt lgkmcnt(8)
	v_mfma_f32_16x16x32_f16 v[18:21], v[116:119], v[40:43], v[14:17]
	s_waitcnt lgkmcnt(6)
	v_mfma_f32_16x16x32_f16 v[14:17], v[76:79], v[40:43], v[30:33]
	s_waitcnt lgkmcnt(4)
	v_mfma_f32_16x16x32_f16 v[10:13], v[84:87], v[40:43], v[2:5]
	s_waitcnt lgkmcnt(2)
	v_mfma_f32_16x16x32_f16 v[2:5], v[100:103], v[40:43], v[34:37]
	s_and_saveexec_b64 s[4:5], vcc
	s_cbranch_execz .LBB2_20
	v_mul_u32_u24_sdwa v26, v61, s7 dst_sel:DWORD dst_unused:UNUSED_PAD src0_sel:WORD_0 src1_sel:DWORD
	v_mul_i32_i24_sdwa v27, v26, s8 dst_sel:DWORD dst_unused:UNUSED_PAD src0_sel:WORD_1 src1_sel:DWORD
	s_waitcnt vmcnt(8)
	v_cvt_pk_f16_f32 v9, v8, v9
	v_cvt_pk_f16_f32 v8, v6, v7
	v_mul_u32_u24_sdwa v6, v26, s6 dst_sel:DWORD dst_unused:UNUSED_PAD src0_sel:WORD_1 src1_sel:DWORD
	v_add_lshl_u32 v7, v27, v61, 3
	v_add3_u32 v6, 0, v6, v7
	ds_write_b64 v6, v[8:9] offset:57600

.LBB2_26:
	s_or_b64 exec, exec, s[0:1]
	s_add_i32 s0, 0, 0x11880
	s_movk_i32 s1, 0x1600
	v_mov_b32_e32 v6, s0
	v_mad_u32_u24 v7, v26, s1, v6
	v_lshlrev_b32_e32 v8, 2, v38
	v_add_u32_e32 v9, v7, v8
	ds_write2st64_b32 v9, v22, v23 offset1:1
	ds_write2st64_b32 v9, v24, v25 offset0:2 offset1:3
	ds_write2st64_b32 v9, v18, v19 offset0:4 offset1:5
	ds_write2st64_b32 v9, v20, v21 offset0:6 offset1:7
	ds_write2st64_b32 v9, v14, v15 offset0:8 offset1:9
	ds_write2st64_b32 v9, v16, v17 offset0:10 offset1:11
	ds_write2st64_b32 v9, v10, v11 offset0:12 offset1:13
	ds_write2st64_b32 v9, v12, v13 offset0:14 offset1:15
	ds_write2st64_b32 v9, v2, v3 offset0:16 offset1:17
	ds_write2st64_b32 v9, v4, v5 offset0:18 offset1:19
	ds_write_b32 v9, v28 offset:5120
	v_xor_b32_e32 v9, 4, v26
	v_mad_u32_u24 v6, v9, s1, v6
	v_add_u32_e32 v29, v6, v8
	s_waitcnt lgkmcnt(0)
	s_barrier
	ds_read_b32 v8, v29 offset:5120
	v_lshlrev_b32_e32 v27, 2, v59
	v_add_u32_e32 v7, v7, v27
	v_add_u32_e32 v6, v6, v27
	ds_read_b32 v31, v6 offset:4224
	ds_read_b32 v30, v7 offset:4224
	ds_read2st64_b32 v[36:37], v29 offset0:18 offset1:19
	s_waitcnt lgkmcnt(3)
	v_max_f32_e32 v6, v8, v8
	v_max_f32_e32 v7, v28, v28
	v_max_f32_e32 v6, v7, v6
	v_sub_f32_e32 v7, v28, v6
	v_sub_f32_e32 v6, v8, v6
	v_exp_f32_e32 v32, v7
	v_exp_f32_e32 v33, v6
	v_lshl_add_u32 v28, v39, 2, 0
	v_add_u32_e32 v51, 0x10e00, v28
	ds_read_b128 v[6:9], v51
	s_waitcnt lgkmcnt(2)
	v_pk_mul_f32 v[30:31], v[30:31], v[32:33]
	s_nop 0
	v_add_f32_e32 v34, v30, v31
	v_rcp_f32_e32 v34, v34
	ds_read2st64_b32 v[30:31], v29 offset0:16 offset1:17
	s_movk_i32 s0, 0xa0
	v_mul_f32_e32 v44, v32, v34
	v_mul_f32_e32 v46, v33, v34
	ds_read2st64_b32 v[32:33], v29 offset1:1
	ds_read2st64_b32 v[34:35], v29 offset0:2 offset1:3
	ds_read2st64_b32 v[40:41], v29 offset0:4 offset1:5
	ds_read2st64_b32 v[42:43], v29 offset0:6 offset1:7
	ds_read2st64_b32 v[48:49], v29 offset0:8 offset1:9
	ds_read2st64_b32 v[52:53], v29 offset0:10 offset1:11
	ds_read2st64_b32 v[54:55], v29 offset0:12 offset1:13
	ds_read2st64_b32 v[62:63], v29 offset0:14 offset1:15
	s_waitcnt lgkmcnt(7)
	v_pk_mul_f32 v[32:33], v[46:47], v[32:33] op_sel_hi:[0,1]
	v_pk_fma_f32 v[22:23], v[44:45], v[22:23], v[32:33] op_sel_hi:[0,1,1]
	v_cvt_pk_f16_f32 v32, v22, v23
	s_waitcnt lgkmcnt(6)
	v_pk_mul_f32 v[22:23], v[46:47], v[34:35] op_sel_hi:[0,1]
	v_pk_fma_f32 v[22:23], v[44:45], v[24:25], v[22:23] op_sel_hi:[0,1,1]
	v_cvt_pk_f16_f32 v33, v22, v23
	s_waitcnt lgkmcnt(5)
	v_pk_mul_f32 v[22:23], v[46:47], v[40:41] op_sel_hi:[0,1]
	v_pk_fma_f32 v[18:19], v[44:45], v[18:19], v[22:23] op_sel_hi:[0,1,1]
	v_cvt_pk_f16_f32 v34, v18, v19
	s_waitcnt lgkmcnt(4)
	v_pk_mul_f32 v[18:19], v[46:47], v[42:43] op_sel_hi:[0,1]
	v_pk_fma_f32 v[18:19], v[44:45], v[20:21], v[18:19] op_sel_hi:[0,1,1]
	v_cvt_pk_f16_f32 v35, v18, v19
	s_waitcnt lgkmcnt(3)
	v_pk_mul_f32 v[18:19], v[46:47], v[48:49] op_sel_hi:[0,1]
	v_pk_fma_f32 v[14:15], v[44:45], v[14:15], v[18:19] op_sel_hi:[0,1,1]
	v_cvt_pk_f16_f32 v40, v14, v15
	s_waitcnt lgkmcnt(2)
	v_pk_mul_f32 v[14:15], v[46:47], v[52:53] op_sel_hi:[0,1]
	v_pk_fma_f32 v[14:15], v[44:45], v[16:17], v[14:15] op_sel_hi:[0,1,1]
	v_cvt_pk_f16_f32 v41, v14, v15
	s_waitcnt lgkmcnt(1)
	v_pk_mul_f32 v[14:15], v[46:47], v[54:55] op_sel_hi:[0,1]
	v_pk_fma_f32 v[10:11], v[44:45], v[10:11], v[14:15] op_sel_hi:[0,1,1]
	v_cvt_pk_f16_f32 v42, v10, v11
	s_waitcnt lgkmcnt(0)
	v_pk_mul_f32 v[10:11], v[46:47], v[62:63] op_sel_hi:[0,1]
	v_pk_fma_f32 v[10:11], v[44:45], v[12:13], v[10:11] op_sel_hi:[0,1,1]
	v_cvt_pk_f16_f32 v43, v10, v11
	v_pk_mul_f32 v[10:11], v[46:47], v[30:31] op_sel_hi:[0,1]
	v_pk_fma_f32 v[2:3], v[44:45], v[2:3], v[10:11] op_sel_hi:[0,1,1]
	v_cvt_pk_f16_f32 v24, v2, v3
	v_pk_mul_f32 v[2:3], v[46:47], v[36:37] op_sel_hi:[0,1]
	v_pk_fma_f32 v[2:3], v[44:45], v[4:5], v[2:3] op_sel_hi:[0,1,1]
	v_or_b32_e32 v30, v39, v60
	v_cvt_pk_f16_f32 v2, v2, v3
	v_cmp_lt_u32_e32 vcc, 31, v38
	v_and_or_b32 v29, v39, 4, v60
	v_mul_u32_u24_e32 v3, 0x50, v30
	v_cndmask_b32_e64 v45, v2, 0, vcc
	v_mad_u32_u24 v2, v29, s0, 0
	v_lshlrev_b32_e32 v36, 3, v59
	v_lshlrev_b32_e32 v48, 1, v3
	v_add_u32_e32 v31, 0xe100, v2
	v_and_b32_e32 v2, 24, v36
	v_add_u32_e32 v49, 0, v48
	v_add_u32_e32 v44, v49, v2
	v_add_u32_e32 v37, v31, v2
	v_add3_u32 v25, 0, v2, v48
	ds_read_b64_tr_b16 v[12:13], v44 offset:60160
	ds_read_b64_tr_b16 v[10:11], v25 offset:57600
	ds_read_b64_tr_b16 v[14:15], v25 offset:62720
	ds_read_b64_tr_b16 v[16:17], v44 offset:65280
	ds_read_b64_tr_b16 v[2:3], v37 offset:10240
	ds_read_b64_tr_b16 v[18:19], v25 offset:57664
	ds_read_b64_tr_b16 v[22:23], v37 offset:10272
	ds_read_b64_tr_b16 v[54:55], v44 offset:60192
	ds_read_b64_tr_b16 v[20:21], v44 offset:60224
	ds_read_b64_tr_b16 v[62:63], v44 offset:60288
	s_waitcnt lgkmcnt(8)
	v_mfma_f32_16x16x32_f16 v[6:9], v[10:13], v[32:35], v[6:9]
	v_mov_b32_e32 v4, 0
	v_mov_b32_e32 v5, v4
	ds_read_b64_tr_b16 v[52:53], v25 offset:57632
	ds_read_b64_tr_b16 v[10:11], v25 offset:62784
	s_waitcnt vmcnt(1)
	ds_read_b64_tr_b16 v[66:67], v44 offset:65312
	ds_read_b64_tr_b16 v[12:13], v44 offset:65344
	ds_read_b64_tr_b16 v[70:71], v44 offset:65408
	s_waitcnt lgkmcnt(11)
	v_mfma_f32_16x16x32_f16 v[6:9], v[14:17], v[40:43], v[6:9]
	v_cndmask_b32_e64 v44, v24, 0, vcc
	v_mov_b32_e32 v46, v4
	v_mov_b32_e32 v47, v4
	v_mov_b32_e32 v24, v4
	v_or_b32_e32 v36, 0x60, v36
	s_waitcnt lgkmcnt(10)
	v_mfma_f32_16x16x32_f16 v[14:17], v[2:5], v[44:47], v[6:9]
	s_nop 2
	ds_read_b128 v[6:9], v51 offset:64
	s_waitcnt vmcnt(0)
	ds_read_b128 v[72:75], v51 offset:128
	ds_read_b64_tr_b16 v[2:3], v37 offset:10304
	ds_read_b64_tr_b16 v[64:65], v25 offset:62752
	ds_read_b64_tr_b16 v[68:69], v25 offset:62848
	ds_read_b64_tr_b16 v[60:61], v25 offset:57728
	v_mov_b32_e32 v25, v4
	s_waitcnt lgkmcnt(5)
	v_mfma_f32_16x16x32_f16 v[6:9], v[52:55], v[32:35], v[6:9]
	v_add3_u32 v48, 0, v36, v48
	v_add_u32_e32 v49, v49, v36
	s_movk_i32 s0, 0xff
	s_waitcnt lgkmcnt(2)
	v_mfma_f32_16x16x32_f16 v[6:9], v[64:67], v[40:43], v[6:9]
	v_cmp_lt_u32_e64 s[0:1], s0, v0
	v_mfma_f32_16x16x32_f16 v[22:25], v[22:25], v[44:47], v[6:9]
	v_mfma_f32_16x16x32_f16 v[6:9], v[18:21], v[32:35], v[72:75]
	ds_read_b64_tr_b16 v[18:19], v48 offset:57600
	ds_read_b64_tr_b16 v[20:21], v49 offset:60160
	v_mfma_f32_16x16x32_f16 v[6:9], v[10:13], v[40:43], v[6:9]
	v_mfma_f32_16x16x32_f16 v[10:13], v[2:5], v[44:47], v[6:9]
	v_add_u32_e32 v2, v31, v36
	s_nop 5
	ds_read_b128 v[6:9], v51 offset:192
	ds_read_b64_tr_b16 v[52:53], v48 offset:62720
	ds_read_b64_tr_b16 v[2:3], v2 offset:10240
	ds_read_b128 v[64:67], v51 offset:256
	ds_read_b64_tr_b16 v[54:55], v49 offset:65280
	s_waitcnt lgkmcnt(4)
	v_mfma_f32_16x16x32_f16 v[6:9], v[18:21], v[32:35], v[6:9]
	s_waitcnt lgkmcnt(0)
	v_mfma_f32_16x16x32_f16 v[6:9], v[52:55], v[40:43], v[6:9]
	v_mfma_f32_16x16x32_f16 v[18:21], v[2:5], v[44:47], v[6:9]
	ds_read_b64_tr_b16 v[2:3], v37 offset:10368
	v_mfma_f32_16x16x32_f16 v[6:9], v[60:63], v[32:35], v[64:67]
	v_mfma_f32_16x16x32_f16 v[6:9], v[68:71], v[40:43], v[6:9]
	s_waitcnt lgkmcnt(0)
	v_mfma_f32_16x16x32_f16 v[6:9], v[2:5], v[44:47], v[6:9]
	s_and_saveexec_b64 s[6:7], s[0:1]
	s_xor_b64 s[0:1], exec, s[6:7]
	s_cbranch_execz .LBB2_38
	v_lshlrev_b32_e32 v5, 2, v1
	s_add_i32 s6, 0, 0x10f40
	v_cvt_pk_f16_f32 v0, v14, v15
	v_add_u32_e32 v14, 0x11840, v28
	v_lshl_add_u32 v5, v5, 1, s6
	v_cvt_pk_f16_f32 v3, v24, v25
	v_cvt_pk_f16_f32 v2, v22, v23
	v_cvt_pk_f16_f32 v15, v20, v21
	v_lshl_add_u32 v28, v30, 5, v5
	ds_read_b128 v[20:23], v14
	ds_read_b64_tr_b16 v[24:25], v28
	ds_read_b64_tr_b16 v[26:27], v28 offset:512
	v_lshl_add_u32 v5, v29, 5, v5
	v_cvt_pk_f16_f32 v1, v16, v17
	v_cvt_pk_f16_f32 v14, v18, v19
	ds_read_b64_tr_b16 v[16:17], v28 offset:1024
	ds_read_b64_tr_b16 v[18:19], v28 offset:1536
	v_cvt_pk_f16_f32 v28, v6, v7
	ds_read_b64_tr_b16 v[6:7], v5 offset:2048
	s_waitcnt lgkmcnt(3)
	v_mfma_f32_16x16x32_f16 v[0:3], v[24:27], v[0:3], v[20:23]
	v_cvt_pk_f16_f32 v13, v12, v13
	v_cvt_pk_f16_f32 v12, v10, v11
	v_cvt_pk_f16_f32 v5, v8, v9
	v_mov_b32_e32 v8, v4
	v_mov_b32_e32 v9, v4
	s_waitcnt lgkmcnt(1)
	v_mfma_f32_16x16x32_f16 v[10:13], v[16:19], v[12:15], v[0:3]
	s_nop 2
	v_cndmask_b32_e64 v3, v5, 0, vcc
	v_cndmask_b32_e64 v2, v28, 0, vcc
	v_mov_b32_e32 v5, v4
	s_waitcnt lgkmcnt(0)
	s_nop 0
	v_mfma_f32_16x16x32_f16 v[0:3], v[6:9], v[2:5], v[10:13]
	s_and_saveexec_b64 s[6:7], s[2:3]
	s_xor_b64 s[2:3], exec, s[6:7]
	s_cbranch_execz .LBB2_35
	v_cmp_ne_u32_e32 vcc, 3, v50
	s_and_saveexec_b64 s[6:7], vcc
	s_cbranch_execz .LBB2_34
	v_cmp_ne_u32_e32 vcc, 1, v50
	s_and_saveexec_b64 s[8:9], vcc
	s_xor_b64 s[8:9], exec, s[8:9]
	v_lshl_add_u32 v4, v56, 1, v56
	v_mov_b32_e32 v5, 0
	v_lshl_add_u64 v[4:5], v[4:5], 2, s[4:5]
	s_mov_b64 s[10:11], 0x70000
	v_lshl_add_u64 v[4:5], v[4:5], 0, s[10:11]
	s_andn2_saveexec_b64 s[8:9], s[8:9]
	v_mul_lo_u32 v4, v56, 7
	v_mov_b32_e32 v5, 0
	v_lshl_add_u64 v[4:5], v[4:5], 2, s[4:5]
	v_lshl_add_u64 v[4:5], v[4:5], 0, 16
	s_or_b64 exec, exec, s[8:9]
	v_max3_f32 v3, v0, v1, v2
	v_sub_f32_e32 v0, v0, v3
	v_sub_f32_e32 v1, v1, v3
	v_mul_f32_e32 v0, 0x3fb8aa3b, v0
	v_mul_f32_e32 v1, 0x3fb8aa3b, v1
	v_sub_f32_e32 v2, v2, v3
	v_exp_f32_e32 v0, v0
	v_exp_f32_e32 v1, v1
	v_mul_f32_e32 v2, 0x3fb8aa3b, v2
	v_exp_f32_e32 v3, v2
	v_add_f32_e32 v2, v0, v1
	v_add_f32_e32 v2, v3, v2
	v_rcp_f32_e32 v2, v2
	s_nop 0
	v_pk_mul_f32 v[0:1], v[0:1], v[2:3] op_sel_hi:[1,0]
	v_mul_f32_e32 v2, v3, v2
	global_store_dwordx3 v[4:5], v[0:2], off nt

.LBB2_35:
	s_andn2_saveexec_b64 s[2:3], s[2:3]
	s_cbranch_execz .LBB2_37
	s_nop 2
	v_mul_f32_e32 v0, 0xbfb8aa3b, v0
	v_mul_f32_e32 v1, 0xbfb8aa3b, v1
	v_mul_f32_e32 v2, 0xbfb8aa3b, v2
	v_mul_f32_e32 v3, 0xbfb8aa3b, v3
	v_exp_f32_e32 v0, v0
	v_exp_f32_e32 v1, v1
	v_exp_f32_e32 v2, v2
	v_exp_f32_e32 v3, v3
	v_mul_lo_u32 v4, v56, 7
	v_mov_b32_e32 v5, 0
	v_pk_add_f32 v[0:1], v[0:1], 1.0 op_sel_hi:[1,0]
	v_pk_add_f32 v[2:3], v[2:3], 1.0 op_sel_hi:[1,0]
	v_lshl_add_u64 v[4:5], v[4:5], 2, s[4:5]
	v_rcp_f32_e32 v0, v0
	v_rcp_f32_e32 v1, v1
	v_rcp_f32_e32 v2, v2
	v_rcp_f32_e32 v3, v3
	s_nop 0
	global_store_dwordx4 v[4:5], v[0:3], off nt
